# attention final combine rewritten: DPP row sums + one cross-lane hop, rows staged through LDS and stored as 8 dwordx4 per lane (was 80 dependent bpermutes and 64 store_short)
# baseline (speedup 1.0000x reference)
; __device__ __forceinline__ float shx(float v, int m, int lane) { return __int_as_float(__builtin_amdgcn_ds_bpermute((lane ^ m) << 2, __float_as_int(v))); }
; __device__ __forceinline__ int accrow(int t, int h) { return (t & 3) + 8 * (t >> 2) + 4 * h; }
; #define INP(i)  ((const float*)(const GAS float*)karg64(8 * (i)))
; __device__ __forceinline__ void attn_unit(const Frame& F, int layer, int qrow0, int ntiles, int b, int head, float lam, float m2, float lam_init) {
;     ...
;     if (mp == 0) {
;         const float* sw = INP(I_SUBLN) + layer * 128;
;         float swv[4];
; #pragma unroll
;         for (int j = 0; j < 4; ++j) swv[j] = sw[32 * j + r32] * lam_init;
; #pragma unroll
;         for (int t = 0; t < 16; ++t) {
;             const int q = accrow(t, hh);
;             float v[4]; float ss = 0.f;
; #pragma unroll
;             for (int j = 0; j < 4; ++j) { v[j] = o[j][t] * isc[t] - X[q * 128 + 32 * j + r32]; ss += v[j] * v[j]; }
; #pragma unroll
;             for (int of = 1; of < 32; of <<= 1) ss += shx(ss, of, lane_e);
.LBB0_555:
	s_andn2_b64 vcc, exec, s[2:3]
	s_waitcnt lgkmcnt(0)
	s_barrier
	s_cbranch_vccnz .LBB0_557
	s_load_dwordx2 s[2:3], s[0:1], 0x78
	s_waitcnt lgkmcnt(0)
	s_lshl_b64 s[10:11], s[48:49], 2
	s_add_u32 s2, s2, s10
	s_addc_u32 s3, s3, s11
	global_load_dword v178, v81, s[2:3] offset:0
	global_load_dword v179, v81, s[2:3] offset:128
	global_load_dword v180, v81, s[2:3] offset:256
	global_load_dword v181, v81, s[2:3] offset:384
	s_lshr_b32 s5, s4, 14
	s_mul_i32 s5, s5, 8704
	s_add_i32 s5, s5, 80000
	s_lshl_b32 s15, s7, 11
	s_add_u32 s42, s40, s30
	s_addc_u32 s43, s41, 0
	s_add_u32 s42, s42, 0x46b34800
	s_addc_u32 s43, s43, 0
	s_add_u32 s42, s42, s15
	s_addc_u32 s43, s43, 0
	v_lshl_add_u32 v182, v82, 11, v81
	v_add_u32_e32 v182, s4, v182
	v_mul_u32_u24_e32 v183, 0x440, v82
	v_lshl_add_u32 v183, v80, 1, v183
	v_add_u32_e32 v183, s5, v183
	v_xor_b32_e32 v184, 64, v86
	v_lshrrev_b32_e32 v187, 4, v193
	v_and_b32_e32 v186, 15, v193
	v_lshlrev_b32_e32 v186, 4, v186
	v_mul_u32_u24_e32 v185, 0x110, v187
	v_add3_u32 v185, v185, v186, s5
	v_lshl_add_u32 v186, v187, 11, v186
	ds_read_b32 v106, v182 offset:0
	ds_read_b32 v107, v182 offset:128
	ds_read_b32 v108, v182 offset:256
	ds_read_b32 v109, v182 offset:384
	ds_read_b32 v110, v182 offset:512
	ds_read_b32 v111, v182 offset:640
	ds_read_b32 v112, v182 offset:768
	ds_read_b32 v113, v182 offset:896
	ds_read_b32 v114, v182 offset:1024
	ds_read_b32 v115, v182 offset:1152
	ds_read_b32 v116, v182 offset:1280
	ds_read_b32 v117, v182 offset:1408
	s_waitcnt lgkmcnt(8)
	v_fma_f32 v106, v32, v76, -v106
	v_fma_f32 v107, v48, v76, -v107
	v_fma_f32 v108, v0, v76, -v108
	v_fma_f32 v109, v16, v76, -v109
	v_mul_f32_e32 v146, v106, v106
	v_fmac_f32_e32 v146, v107, v107
	v_fmac_f32_e32 v146, v108, v108
	v_fmac_f32_e32 v146, v109, v109
	ds_read_b32 v118, v182 offset:1536
	ds_read_b32 v119, v182 offset:1664
	ds_read_b32 v120, v182 offset:1792
	ds_read_b32 v121, v182 offset:1920
	s_waitcnt lgkmcnt(8)
	v_fma_f32 v110, v33, v77, -v110
	v_fma_f32 v111, v49, v77, -v111
	v_fma_f32 v112, v1, v77, -v112
	v_fma_f32 v113, v17, v77, -v113
	v_mul_f32_e32 v147, v110, v110
	v_fmac_f32_e32 v147, v111, v111
	v_fmac_f32_e32 v147, v112, v112
	v_fmac_f32_e32 v147, v113, v113
	ds_read_b32 v122, v182 offset:4096
	ds_read_b32 v123, v182 offset:4224
	ds_read_b32 v124, v182 offset:4352
	ds_read_b32 v125, v182 offset:4480
	s_waitcnt lgkmcnt(8)
	v_fma_f32 v114, v34, v78, -v114
	v_fma_f32 v115, v50, v78, -v115
	v_fma_f32 v116, v2, v78, -v116
	v_fma_f32 v117, v18, v78, -v117
	v_mul_f32_e32 v148, v114, v114
	v_fmac_f32_e32 v148, v115, v115
	v_fmac_f32_e32 v148, v116, v116
	v_fmac_f32_e32 v148, v117, v117
	ds_read_b32 v126, v182 offset:4608
	ds_read_b32 v127, v182 offset:4736
	ds_read_b32 v128, v182 offset:4864
	ds_read_b32 v129, v182 offset:4992
	s_waitcnt lgkmcnt(8)
	v_fma_f32 v118, v35, v79, -v118
	v_fma_f32 v119, v51, v79, -v119
	v_fma_f32 v120, v3, v79, -v120
	v_fma_f32 v121, v19, v79, -v121
	v_mul_f32_e32 v149, v118, v118
	v_fmac_f32_e32 v149, v119, v119
	v_fmac_f32_e32 v149, v120, v120
	v_fmac_f32_e32 v149, v121, v121
	ds_read_b32 v130, v182 offset:5120
	ds_read_b32 v131, v182 offset:5248
	ds_read_b32 v132, v182 offset:5376
	ds_read_b32 v133, v182 offset:5504
	s_waitcnt lgkmcnt(8)
	v_fma_f32 v122, v36, v72, -v122
	v_fma_f32 v123, v52, v72, -v123
	v_fma_f32 v124, v4, v72, -v124
	v_fma_f32 v125, v20, v72, -v125
	v_mul_f32_e32 v150, v122, v122
	v_fmac_f32_e32 v150, v123, v123
	v_fmac_f32_e32 v150, v124, v124
	v_fmac_f32_e32 v150, v125, v125
	ds_read_b32 v134, v182 offset:5632
	ds_read_b32 v135, v182 offset:5760
	ds_read_b32 v136, v182 offset:5888
	ds_read_b32 v137, v182 offset:6016
	s_waitcnt lgkmcnt(8)
	v_fma_f32 v126, v37, v73, -v126
	v_fma_f32 v127, v53, v73, -v127
	v_fma_f32 v128, v5, v73, -v128
	v_fma_f32 v129, v21, v73, -v129
	v_mul_f32_e32 v151, v126, v126
	v_fmac_f32_e32 v151, v127, v127
	v_fmac_f32_e32 v151, v128, v128
	v_fmac_f32_e32 v151, v129, v129
	s_waitcnt lgkmcnt(4)
	v_fma_f32 v130, v38, v74, -v130
	v_fma_f32 v131, v54, v74, -v131
	v_fma_f32 v132, v6, v74, -v132
	v_fma_f32 v133, v22, v74, -v133
	v_mul_f32_e32 v152, v130, v130
	v_fmac_f32_e32 v152, v131, v131
	v_fmac_f32_e32 v152, v132, v132
	v_fmac_f32_e32 v152, v133, v133
	s_waitcnt lgkmcnt(0)
; __device__ __forceinline__ unsigned short f2bf(float f) { return (unsigned short)(pk2(f, 0.f) & 0xffffu); }
; __device__ __forceinline__ float shx(float v, int m, int lane) { return __int_as_float(__builtin_amdgcn_ds_bpermute((lane ^ m) << 2, __float_as_int(v))); }
; __device__ __forceinline__ int accrow(int t, int h) { return (t & 3) + 8 * (t >> 2) + 4 * h; }
; __device__ __forceinline__ void attn_unit(const Frame& F, int layer, int qrow0, int ntiles, int b, int head, float lam, float m2, float lam_init) {
;     ...
;         for (int t = 0; t < 16; ++t) {
;             const int q = accrow(t, hh);
;             float v[4]; float ss = 0.f;
; #pragma unroll
;             for (int j = 0; j < 4; ++j) { v[j] = o[j][t] * isc[t] - X[q * 128 + 32 * j + r32]; ss += v[j] * v[j]; }
; #pragma unroll
;             for (int of = 1; of < 32; of <<= 1) ss += shx(ss, of, lane_e);
;             const float rstd = rsqrtf(ss * (1.f / 128.f) + EPS);
;             bf16_t* op = A2p + (size_t)(qrow0 + 32 * qg + q) * 1024 + head * 128 + r32;
; #pragma unroll
;             for (int j = 0; j < 4; ++j) op[32 * j] = f2bf(v[j] * rstd * swv[j]);
	v_fma_f32 v134, v39, v75, -v134
	v_fma_f32 v135, v55, v75, -v135
	v_fma_f32 v136, v7, v75, -v136
	v_fma_f32 v137, v23, v75, -v137
	v_mul_f32_e32 v153, v134, v134
	v_fmac_f32_e32 v153, v135, v135
	v_fmac_f32_e32 v153, v136, v136
	v_fmac_f32_e32 v153, v137, v137
	v_add_f32_dpp v146, v146, v146 quad_perm:[1,0,3,2] row_mask:0xf bank_mask:0xf bound_ctrl:1
	v_add_f32_dpp v147, v147, v147 quad_perm:[1,0,3,2] row_mask:0xf bank_mask:0xf bound_ctrl:1
	v_add_f32_dpp v148, v148, v148 quad_perm:[1,0,3,2] row_mask:0xf bank_mask:0xf bound_ctrl:1
	v_add_f32_dpp v149, v149, v149 quad_perm:[1,0,3,2] row_mask:0xf bank_mask:0xf bound_ctrl:1
	v_add_f32_dpp v150, v150, v150 quad_perm:[1,0,3,2] row_mask:0xf bank_mask:0xf bound_ctrl:1
	v_add_f32_dpp v151, v151, v151 quad_perm:[1,0,3,2] row_mask:0xf bank_mask:0xf bound_ctrl:1
	v_add_f32_dpp v152, v152, v152 quad_perm:[1,0,3,2] row_mask:0xf bank_mask:0xf bound_ctrl:1
	v_add_f32_dpp v153, v153, v153 quad_perm:[1,0,3,2] row_mask:0xf bank_mask:0xf bound_ctrl:1
	v_add_f32_dpp v146, v146, v146 quad_perm:[2,3,0,1] row_mask:0xf bank_mask:0xf bound_ctrl:1
	v_add_f32_dpp v147, v147, v147 quad_perm:[2,3,0,1] row_mask:0xf bank_mask:0xf bound_ctrl:1
	v_add_f32_dpp v148, v148, v148 quad_perm:[2,3,0,1] row_mask:0xf bank_mask:0xf bound_ctrl:1
	v_add_f32_dpp v149, v149, v149 quad_perm:[2,3,0,1] row_mask:0xf bank_mask:0xf bound_ctrl:1
	v_add_f32_dpp v150, v150, v150 quad_perm:[2,3,0,1] row_mask:0xf bank_mask:0xf bound_ctrl:1
	v_add_f32_dpp v151, v151, v151 quad_perm:[2,3,0,1] row_mask:0xf bank_mask:0xf bound_ctrl:1
	v_add_f32_dpp v152, v152, v152 quad_perm:[2,3,0,1] row_mask:0xf bank_mask:0xf bound_ctrl:1
	v_add_f32_dpp v153, v153, v153 quad_perm:[2,3,0,1] row_mask:0xf bank_mask:0xf bound_ctrl:1
	v_add_f32_dpp v146, v146, v146 row_half_mirror row_mask:0xf bank_mask:0xf bound_ctrl:1
	v_add_f32_dpp v147, v147, v147 row_half_mirror row_mask:0xf bank_mask:0xf bound_ctrl:1
	v_add_f32_dpp v148, v148, v148 row_half_mirror row_mask:0xf bank_mask:0xf bound_ctrl:1
	v_add_f32_dpp v149, v149, v149 row_half_mirror row_mask:0xf bank_mask:0xf bound_ctrl:1
	v_add_f32_dpp v150, v150, v150 row_half_mirror row_mask:0xf bank_mask:0xf bound_ctrl:1
	v_add_f32_dpp v151, v151, v151 row_half_mirror row_mask:0xf bank_mask:0xf bound_ctrl:1
	v_add_f32_dpp v152, v152, v152 row_half_mirror row_mask:0xf bank_mask:0xf bound_ctrl:1
	v_add_f32_dpp v153, v153, v153 row_half_mirror row_mask:0xf bank_mask:0xf bound_ctrl:1
	v_add_f32_dpp v146, v146, v146 row_mirror row_mask:0xf bank_mask:0xf bound_ctrl:1
	v_add_f32_dpp v147, v147, v147 row_mirror row_mask:0xf bank_mask:0xf bound_ctrl:1
	v_add_f32_dpp v148, v148, v148 row_mirror row_mask:0xf bank_mask:0xf bound_ctrl:1
	v_add_f32_dpp v149, v149, v149 row_mirror row_mask:0xf bank_mask:0xf bound_ctrl:1
	v_add_f32_dpp v150, v150, v150 row_mirror row_mask:0xf bank_mask:0xf bound_ctrl:1
	v_add_f32_dpp v151, v151, v151 row_mirror row_mask:0xf bank_mask:0xf bound_ctrl:1
	v_add_f32_dpp v152, v152, v152 row_mirror row_mask:0xf bank_mask:0xf bound_ctrl:1
	v_add_f32_dpp v153, v153, v153 row_mirror row_mask:0xf bank_mask:0xf bound_ctrl:1
	ds_bpermute_b32 v154, v184, v146
	ds_bpermute_b32 v155, v184, v147
	ds_bpermute_b32 v156, v184, v148
	ds_bpermute_b32 v157, v184, v149
	ds_bpermute_b32 v158, v184, v150
	ds_bpermute_b32 v159, v184, v151
	ds_bpermute_b32 v160, v184, v152
	ds_bpermute_b32 v161, v184, v153
	s_waitcnt vmcnt(0)
	v_mul_f32_e32 v178, s18, v178
	v_mul_f32_e32 v179, s18, v179
	v_mul_f32_e32 v180, s18, v180
	v_mul_f32_e32 v181, s18, v181
	s_waitcnt lgkmcnt(7)
	v_add_f32_e32 v146, v146, v154
	s_waitcnt lgkmcnt(6)
	v_add_f32_e32 v147, v147, v155
	s_waitcnt lgkmcnt(5)
	v_add_f32_e32 v148, v148, v156
	s_waitcnt lgkmcnt(4)
	v_add_f32_e32 v149, v149, v157
	s_waitcnt lgkmcnt(3)
	v_add_f32_e32 v150, v150, v158
	s_waitcnt lgkmcnt(2)
	v_add_f32_e32 v151, v151, v159
	s_waitcnt lgkmcnt(1)
	v_add_f32_e32 v152, v152, v160
	s_waitcnt lgkmcnt(0)
	v_add_f32_e32 v153, v153, v161
	v_mov_b32_e32 v187, 0x3c000000
	v_fmaak_f32 v146, v146, v187, 0x358637bd
	v_fmaak_f32 v147, v147, v187, 0x358637bd
	v_fmaak_f32 v148, v148, v187, 0x358637bd
	v_fmaak_f32 v149, v149, v187, 0x358637bd
	v_fmaak_f32 v150, v150, v187, 0x358637bd
	v_fmaak_f32 v151, v151, v187, 0x358637bd
	v_fmaak_f32 v152, v152, v187, 0x358637bd
	v_fmaak_f32 v153, v153, v187, 0x358637bd
	v_rsq_f32_e32 v146, v146
	v_rsq_f32_e32 v147, v147
	v_rsq_f32_e32 v148, v148
	v_rsq_f32_e32 v149, v149
	v_rsq_f32_e32 v150, v150
	v_rsq_f32_e32 v151, v151
	v_rsq_f32_e32 v152, v152
	v_rsq_f32_e32 v153, v153
	s_nop 0
	v_mul_f32_e32 v106, v106, v146
	v_mul_f32_e32 v107, v107, v146
	v_mul_f32_e32 v108, v108, v146
	v_mul_f32_e32 v109, v109, v146
	v_mul_f32_e32 v106, v178, v106
	v_mul_f32_e32 v107, v179, v107
	v_mul_f32_e32 v108, v180, v108
	v_mul_f32_e32 v109, v181, v109
	v_cvt_pk_bf16_f32 v106, v106, v106
	v_cvt_pk_bf16_f32 v107, v107, v107
	v_cvt_pk_bf16_f32 v108, v108, v108
	v_cvt_pk_bf16_f32 v109, v109, v109
	ds_write_b16 v183, v106 offset:0
	ds_write_b16 v183, v107 offset:64
	ds_write_b16 v183, v108 offset:128
	ds_write_b16 v183, v109 offset:192
	v_mul_f32_e32 v110, v110, v147
	v_mul_f32_e32 v111, v111, v147
	v_mul_f32_e32 v112, v112, v147
	v_mul_f32_e32 v113, v113, v147
	v_mul_f32_e32 v110, v178, v110
	v_mul_f32_e32 v111, v179, v111
	v_mul_f32_e32 v112, v180, v112
	v_mul_f32_e32 v113, v181, v113
	v_cvt_pk_bf16_f32 v110, v110, v110
	v_cvt_pk_bf16_f32 v111, v111, v111
	v_cvt_pk_bf16_f32 v112, v112, v112
	v_cvt_pk_bf16_f32 v113, v113, v113
	ds_write_b16 v183, v110 offset:272
	ds_write_b16 v183, v111 offset:336
	ds_write_b16 v183, v112 offset:400
	ds_write_b16 v183, v113 offset:464
	v_mul_f32_e32 v114, v114, v148
	v_mul_f32_e32 v115, v115, v148
	v_mul_f32_e32 v116, v116, v148
	v_mul_f32_e32 v117, v117, v148
	v_mul_f32_e32 v114, v178, v114
	v_mul_f32_e32 v115, v179, v115
	v_mul_f32_e32 v116, v180, v116
	v_mul_f32_e32 v117, v181, v117
	v_cvt_pk_bf16_f32 v114, v114, v114
	v_cvt_pk_bf16_f32 v115, v115, v115
	v_cvt_pk_bf16_f32 v116, v116, v116
	v_cvt_pk_bf16_f32 v117, v117, v117
	ds_write_b16 v183, v114 offset:544
	ds_write_b16 v183, v115 offset:608
	ds_write_b16 v183, v116 offset:672
	ds_write_b16 v183, v117 offset:736
	v_mul_f32_e32 v118, v118, v149
	v_mul_f32_e32 v119, v119, v149
	v_mul_f32_e32 v120, v120, v149
	v_mul_f32_e32 v121, v121, v149
	v_mul_f32_e32 v118, v178, v118
	v_mul_f32_e32 v119, v179, v119
	v_mul_f32_e32 v120, v180, v120
	v_mul_f32_e32 v121, v181, v121
	v_cvt_pk_bf16_f32 v118, v118, v118
	v_cvt_pk_bf16_f32 v119, v119, v119
	v_cvt_pk_bf16_f32 v120, v120, v120
	v_cvt_pk_bf16_f32 v121, v121, v121
	ds_write_b16 v183, v118 offset:816
	ds_write_b16 v183, v119 offset:880
	ds_write_b16 v183, v120 offset:944
	s_waitcnt lgkmcnt(14)
; __device__ __forceinline__ unsigned short f2bf(float f) { return (unsigned short)(pk2(f, 0.f) & 0xffffu); }
; __device__ __forceinline__ float shx(float v, int m, int lane) { return __int_as_float(__builtin_amdgcn_ds_bpermute((lane ^ m) << 2, __float_as_int(v))); }
; __device__ __forceinline__ int accrow(int t, int h) { return (t & 3) + 8 * (t >> 2) + 4 * h; }
; __device__ __forceinline__ void attn_unit(const Frame& F, int layer, int qrow0, int ntiles, int b, int head, float lam, float m2, float lam_init) {
;     ...
;         for (int t = 0; t < 16; ++t) {
;             const int q = accrow(t, hh);
;             float v[4]; float ss = 0.f;
; #pragma unroll
;             for (int j = 0; j < 4; ++j) { v[j] = o[j][t] * isc[t] - X[q * 128 + 32 * j + r32]; ss += v[j] * v[j]; }
; #pragma unroll
;             for (int of = 1; of < 32; of <<= 1) ss += shx(ss, of, lane_e);
;             const float rstd = rsqrtf(ss * (1.f / 128.f) + EPS);
;             bf16_t* op = A2p + (size_t)(qrow0 + 32 * qg + q) * 1024 + head * 128 + r32;
; #pragma unroll
;             for (int j = 0; j < 4; ++j) op[32 * j] = f2bf(v[j] * rstd * swv[j]);
	ds_write_b16 v183, v121 offset:1008
	v_mul_f32_e32 v122, v122, v150
	v_mul_f32_e32 v123, v123, v150
	v_mul_f32_e32 v124, v124, v150
	v_mul_f32_e32 v125, v125, v150
	v_mul_f32_e32 v122, v178, v122
	v_mul_f32_e32 v123, v179, v123
	v_mul_f32_e32 v124, v180, v124
	v_mul_f32_e32 v125, v181, v125
	v_cvt_pk_bf16_f32 v122, v122, v122
	v_cvt_pk_bf16_f32 v123, v123, v123
	v_cvt_pk_bf16_f32 v124, v124, v124
	v_cvt_pk_bf16_f32 v125, v125, v125
	s_waitcnt lgkmcnt(14)
	ds_write_b16 v183, v122 offset:2176
	s_waitcnt lgkmcnt(14)
	ds_write_b16 v183, v123 offset:2240
	s_waitcnt lgkmcnt(14)
	ds_write_b16 v183, v124 offset:2304
	s_waitcnt lgkmcnt(14)
	ds_write_b16 v183, v125 offset:2368
	v_mul_f32_e32 v126, v126, v151
	v_mul_f32_e32 v127, v127, v151
	v_mul_f32_e32 v128, v128, v151
	v_mul_f32_e32 v129, v129, v151
	v_mul_f32_e32 v126, v178, v126
	v_mul_f32_e32 v127, v179, v127
	v_mul_f32_e32 v128, v180, v128
	v_mul_f32_e32 v129, v181, v129
	v_cvt_pk_bf16_f32 v126, v126, v126
	v_cvt_pk_bf16_f32 v127, v127, v127
	v_cvt_pk_bf16_f32 v128, v128, v128
	v_cvt_pk_bf16_f32 v129, v129, v129
	s_waitcnt lgkmcnt(14)
	ds_write_b16 v183, v126 offset:2448
	s_waitcnt lgkmcnt(14)
	ds_write_b16 v183, v127 offset:2512
	s_waitcnt lgkmcnt(14)
	ds_write_b16 v183, v128 offset:2576
	s_waitcnt lgkmcnt(14)
	ds_write_b16 v183, v129 offset:2640
	v_mul_f32_e32 v130, v130, v152
	v_mul_f32_e32 v131, v131, v152
	v_mul_f32_e32 v132, v132, v152
	v_mul_f32_e32 v133, v133, v152
	v_mul_f32_e32 v130, v178, v130
	v_mul_f32_e32 v131, v179, v131
	v_mul_f32_e32 v132, v180, v132
	v_mul_f32_e32 v133, v181, v133
	v_cvt_pk_bf16_f32 v130, v130, v130
	v_cvt_pk_bf16_f32 v131, v131, v131
	v_cvt_pk_bf16_f32 v132, v132, v132
	v_cvt_pk_bf16_f32 v133, v133, v133
	s_waitcnt lgkmcnt(14)
	ds_write_b16 v183, v130 offset:2720
	s_waitcnt lgkmcnt(14)
	ds_write_b16 v183, v131 offset:2784
	s_waitcnt lgkmcnt(14)
	ds_write_b16 v183, v132 offset:2848
	s_waitcnt lgkmcnt(14)
	ds_write_b16 v183, v133 offset:2912
	v_mul_f32_e32 v134, v134, v153
	v_mul_f32_e32 v135, v135, v153
	v_mul_f32_e32 v136, v136, v153
	v_mul_f32_e32 v137, v137, v153
	v_mul_f32_e32 v134, v178, v134
	v_mul_f32_e32 v135, v179, v135
	v_mul_f32_e32 v136, v180, v136
	v_mul_f32_e32 v137, v181, v137
	v_cvt_pk_bf16_f32 v134, v134, v134
	v_cvt_pk_bf16_f32 v135, v135, v135
	v_cvt_pk_bf16_f32 v136, v136, v136
	v_cvt_pk_bf16_f32 v137, v137, v137
	s_waitcnt lgkmcnt(14)
	ds_write_b16 v183, v134 offset:2992
	s_waitcnt lgkmcnt(14)
	ds_write_b16 v183, v135 offset:3056
	s_waitcnt lgkmcnt(14)
	ds_write_b16 v183, v136 offset:3120
	s_waitcnt lgkmcnt(14)
	ds_write_b16 v183, v137 offset:3184
	s_waitcnt lgkmcnt(0)
	ds_read_b32 v106, v182 offset:8192
	ds_read_b32 v107, v182 offset:8320
	ds_read_b32 v108, v182 offset:8448
	ds_read_b32 v109, v182 offset:8576
	ds_read_b32 v110, v182 offset:8704
	ds_read_b32 v111, v182 offset:8832
	ds_read_b32 v112, v182 offset:8960
	ds_read_b32 v113, v182 offset:9088
	ds_read_b32 v114, v182 offset:9216
	ds_read_b32 v115, v182 offset:9344
	ds_read_b32 v116, v182 offset:9472
	ds_read_b32 v117, v182 offset:9600
	s_waitcnt lgkmcnt(8)
	v_fma_f32 v106, v40, v68, -v106
	v_fma_f32 v107, v56, v68, -v107
	v_fma_f32 v108, v8, v68, -v108
	v_fma_f32 v109, v24, v68, -v109
	v_mul_f32_e32 v146, v106, v106
	v_fmac_f32_e32 v146, v107, v107
	v_fmac_f32_e32 v146, v108, v108
	v_fmac_f32_e32 v146, v109, v109
	ds_read_b32 v118, v182 offset:9728
	ds_read_b32 v119, v182 offset:9856
	ds_read_b32 v120, v182 offset:9984
	ds_read_b32 v121, v182 offset:10112
	s_waitcnt lgkmcnt(8)
	v_fma_f32 v110, v41, v69, -v110
	v_fma_f32 v111, v57, v69, -v111
	v_fma_f32 v112, v9, v69, -v112
	v_fma_f32 v113, v25, v69, -v113
	v_mul_f32_e32 v147, v110, v110
	v_fmac_f32_e32 v147, v111, v111
	v_fmac_f32_e32 v147, v112, v112
	v_fmac_f32_e32 v147, v113, v113
	ds_read_b32 v122, v182 offset:12288
	ds_read_b32 v123, v182 offset:12416
	ds_read_b32 v124, v182 offset:12544
	ds_read_b32 v125, v182 offset:12672
	s_waitcnt lgkmcnt(8)
	v_fma_f32 v114, v42, v70, -v114
	v_fma_f32 v115, v58, v70, -v115
	v_fma_f32 v116, v10, v70, -v116
	v_fma_f32 v117, v26, v70, -v117
	v_mul_f32_e32 v148, v114, v114
	v_fmac_f32_e32 v148, v115, v115
	v_fmac_f32_e32 v148, v116, v116
	v_fmac_f32_e32 v148, v117, v117
	ds_read_b32 v126, v182 offset:12800
	ds_read_b32 v127, v182 offset:12928
	ds_read_b32 v128, v182 offset:13056
	ds_read_b32 v129, v182 offset:13184
	s_waitcnt lgkmcnt(8)
	v_fma_f32 v118, v43, v71, -v118
	v_fma_f32 v119, v59, v71, -v119
	v_fma_f32 v120, v11, v71, -v120
	v_fma_f32 v121, v27, v71, -v121
	v_mul_f32_e32 v149, v118, v118
	v_fmac_f32_e32 v149, v119, v119
	v_fmac_f32_e32 v149, v120, v120
	v_fmac_f32_e32 v149, v121, v121
	ds_read_b32 v130, v182 offset:13312
	ds_read_b32 v131, v182 offset:13440
	ds_read_b32 v132, v182 offset:13568
	ds_read_b32 v133, v182 offset:13696
	s_waitcnt lgkmcnt(8)
	v_fma_f32 v122, v44, v64, -v122
	v_fma_f32 v123, v60, v64, -v123
	v_fma_f32 v124, v12, v64, -v124
	v_fma_f32 v125, v28, v64, -v125
	v_mul_f32_e32 v150, v122, v122
	v_fmac_f32_e32 v150, v123, v123
	v_fmac_f32_e32 v150, v124, v124
	v_fmac_f32_e32 v150, v125, v125
	ds_read_b32 v134, v182 offset:13824
	ds_read_b32 v135, v182 offset:13952
	ds_read_b32 v136, v182 offset:14080
	ds_read_b32 v137, v182 offset:14208
	s_waitcnt lgkmcnt(8)
	v_fma_f32 v126, v45, v65, -v126
	v_fma_f32 v127, v61, v65, -v127
	v_fma_f32 v128, v13, v65, -v128
	v_fma_f32 v129, v29, v65, -v129
	v_mul_f32_e32 v151, v126, v126
	v_fmac_f32_e32 v151, v127, v127
	v_fmac_f32_e32 v151, v128, v128
	v_fmac_f32_e32 v151, v129, v129
	s_waitcnt lgkmcnt(4)
; __device__ __forceinline__ float shx(float v, int m, int lane) { return __int_as_float(__builtin_amdgcn_ds_bpermute((lane ^ m) << 2, __float_as_int(v))); }
; __device__ __forceinline__ int accrow(int t, int h) { return (t & 3) + 8 * (t >> 2) + 4 * h; }
; __device__ __forceinline__ void attn_unit(const Frame& F, int layer, int qrow0, int ntiles, int b, int head, float lam, float m2, float lam_init) {
;     ...
;         for (int t = 0; t < 16; ++t) {
;             const int q = accrow(t, hh);
;             float v[4]; float ss = 0.f;
; #pragma unroll
;             for (int j = 0; j < 4; ++j) { v[j] = o[j][t] * isc[t] - X[q * 128 + 32 * j + r32]; ss += v[j] * v[j]; }
; #pragma unroll
;             for (int of = 1; of < 32; of <<= 1) ss += shx(ss, of, lane_e);
;             const float rstd = rsqrtf(ss * (1.f / 128.f) + EPS);
	v_fma_f32 v130, v46, v66, -v130
	v_fma_f32 v131, v62, v66, -v131
	v_fma_f32 v132, v14, v66, -v132
	v_fma_f32 v133, v30, v66, -v133
	v_mul_f32_e32 v152, v130, v130
	v_fmac_f32_e32 v152, v131, v131
	v_fmac_f32_e32 v152, v132, v132
	v_fmac_f32_e32 v152, v133, v133
	s_waitcnt lgkmcnt(0)
	v_fma_f32 v134, v47, v67, -v134
	v_fma_f32 v135, v63, v67, -v135
	v_fma_f32 v136, v15, v67, -v136
	v_fma_f32 v137, v31, v67, -v137
	v_mul_f32_e32 v153, v134, v134
	v_fmac_f32_e32 v153, v135, v135
	v_fmac_f32_e32 v153, v136, v136
	v_fmac_f32_e32 v153, v137, v137
	v_add_f32_dpp v146, v146, v146 quad_perm:[1,0,3,2] row_mask:0xf bank_mask:0xf bound_ctrl:1
	v_add_f32_dpp v147, v147, v147 quad_perm:[1,0,3,2] row_mask:0xf bank_mask:0xf bound_ctrl:1
	v_add_f32_dpp v148, v148, v148 quad_perm:[1,0,3,2] row_mask:0xf bank_mask:0xf bound_ctrl:1
	v_add_f32_dpp v149, v149, v149 quad_perm:[1,0,3,2] row_mask:0xf bank_mask:0xf bound_ctrl:1
	v_add_f32_dpp v150, v150, v150 quad_perm:[1,0,3,2] row_mask:0xf bank_mask:0xf bound_ctrl:1
	v_add_f32_dpp v151, v151, v151 quad_perm:[1,0,3,2] row_mask:0xf bank_mask:0xf bound_ctrl:1
	v_add_f32_dpp v152, v152, v152 quad_perm:[1,0,3,2] row_mask:0xf bank_mask:0xf bound_ctrl:1
	v_add_f32_dpp v153, v153, v153 quad_perm:[1,0,3,2] row_mask:0xf bank_mask:0xf bound_ctrl:1
	v_add_f32_dpp v146, v146, v146 quad_perm:[2,3,0,1] row_mask:0xf bank_mask:0xf bound_ctrl:1
	v_add_f32_dpp v147, v147, v147 quad_perm:[2,3,0,1] row_mask:0xf bank_mask:0xf bound_ctrl:1
	v_add_f32_dpp v148, v148, v148 quad_perm:[2,3,0,1] row_mask:0xf bank_mask:0xf bound_ctrl:1
	v_add_f32_dpp v149, v149, v149 quad_perm:[2,3,0,1] row_mask:0xf bank_mask:0xf bound_ctrl:1
	v_add_f32_dpp v150, v150, v150 quad_perm:[2,3,0,1] row_mask:0xf bank_mask:0xf bound_ctrl:1
	v_add_f32_dpp v151, v151, v151 quad_perm:[2,3,0,1] row_mask:0xf bank_mask:0xf bound_ctrl:1
	v_add_f32_dpp v152, v152, v152 quad_perm:[2,3,0,1] row_mask:0xf bank_mask:0xf bound_ctrl:1
	v_add_f32_dpp v153, v153, v153 quad_perm:[2,3,0,1] row_mask:0xf bank_mask:0xf bound_ctrl:1
	v_add_f32_dpp v146, v146, v146 row_half_mirror row_mask:0xf bank_mask:0xf bound_ctrl:1
	v_add_f32_dpp v147, v147, v147 row_half_mirror row_mask:0xf bank_mask:0xf bound_ctrl:1
	v_add_f32_dpp v148, v148, v148 row_half_mirror row_mask:0xf bank_mask:0xf bound_ctrl:1
	v_add_f32_dpp v149, v149, v149 row_half_mirror row_mask:0xf bank_mask:0xf bound_ctrl:1
	v_add_f32_dpp v150, v150, v150 row_half_mirror row_mask:0xf bank_mask:0xf bound_ctrl:1
	v_add_f32_dpp v151, v151, v151 row_half_mirror row_mask:0xf bank_mask:0xf bound_ctrl:1
	v_add_f32_dpp v152, v152, v152 row_half_mirror row_mask:0xf bank_mask:0xf bound_ctrl:1
	v_add_f32_dpp v153, v153, v153 row_half_mirror row_mask:0xf bank_mask:0xf bound_ctrl:1
	v_add_f32_dpp v146, v146, v146 row_mirror row_mask:0xf bank_mask:0xf bound_ctrl:1
	v_add_f32_dpp v147, v147, v147 row_mirror row_mask:0xf bank_mask:0xf bound_ctrl:1
	v_add_f32_dpp v148, v148, v148 row_mirror row_mask:0xf bank_mask:0xf bound_ctrl:1
	v_add_f32_dpp v149, v149, v149 row_mirror row_mask:0xf bank_mask:0xf bound_ctrl:1
	v_add_f32_dpp v150, v150, v150 row_mirror row_mask:0xf bank_mask:0xf bound_ctrl:1
	v_add_f32_dpp v151, v151, v151 row_mirror row_mask:0xf bank_mask:0xf bound_ctrl:1
	v_add_f32_dpp v152, v152, v152 row_mirror row_mask:0xf bank_mask:0xf bound_ctrl:1
	v_add_f32_dpp v153, v153, v153 row_mirror row_mask:0xf bank_mask:0xf bound_ctrl:1
	ds_bpermute_b32 v154, v184, v146
	ds_bpermute_b32 v155, v184, v147
	ds_bpermute_b32 v156, v184, v148
	ds_bpermute_b32 v157, v184, v149
	ds_bpermute_b32 v158, v184, v150
	ds_bpermute_b32 v159, v184, v151
	ds_bpermute_b32 v160, v184, v152
	ds_bpermute_b32 v161, v184, v153
	s_waitcnt lgkmcnt(7)
	v_add_f32_e32 v146, v146, v154
	s_waitcnt lgkmcnt(6)
	v_add_f32_e32 v147, v147, v155
	s_waitcnt lgkmcnt(5)
	v_add_f32_e32 v148, v148, v156
	s_waitcnt lgkmcnt(4)
	v_add_f32_e32 v149, v149, v157
	s_waitcnt lgkmcnt(3)
	v_add_f32_e32 v150, v150, v158
	s_waitcnt lgkmcnt(2)
	v_add_f32_e32 v151, v151, v159
	s_waitcnt lgkmcnt(1)
	v_add_f32_e32 v152, v152, v160
	s_waitcnt lgkmcnt(0)
; __device__ __forceinline__ unsigned short f2bf(float f) { return (unsigned short)(pk2(f, 0.f) & 0xffffu); }
; __device__ __forceinline__ float shx(float v, int m, int lane) { return __int_as_float(__builtin_amdgcn_ds_bpermute((lane ^ m) << 2, __float_as_int(v))); }
; __device__ __forceinline__ int accrow(int t, int h) { return (t & 3) + 8 * (t >> 2) + 4 * h; }
; __device__ __forceinline__ void attn_unit(const Frame& F, int layer, int qrow0, int ntiles, int b, int head, float lam, float m2, float lam_init) {
;     ...
;         for (int t = 0; t < 16; ++t) {
;             const int q = accrow(t, hh);
;             float v[4]; float ss = 0.f;
; #pragma unroll
;             for (int j = 0; j < 4; ++j) { v[j] = o[j][t] * isc[t] - X[q * 128 + 32 * j + r32]; ss += v[j] * v[j]; }
; #pragma unroll
;             for (int of = 1; of < 32; of <<= 1) ss += shx(ss, of, lane_e);
;             const float rstd = rsqrtf(ss * (1.f / 128.f) + EPS);
;             bf16_t* op = A2p + (size_t)(qrow0 + 32 * qg + q) * 1024 + head * 128 + r32;
; #pragma unroll
;             for (int j = 0; j < 4; ++j) op[32 * j] = f2bf(v[j] * rstd * swv[j]);
;         }
	v_add_f32_e32 v153, v153, v161
	v_mov_b32_e32 v187, 0x3c000000
	v_fmaak_f32 v146, v146, v187, 0x358637bd
	v_fmaak_f32 v147, v147, v187, 0x358637bd
	v_fmaak_f32 v148, v148, v187, 0x358637bd
	v_fmaak_f32 v149, v149, v187, 0x358637bd
	v_fmaak_f32 v150, v150, v187, 0x358637bd
	v_fmaak_f32 v151, v151, v187, 0x358637bd
	v_fmaak_f32 v152, v152, v187, 0x358637bd
	v_fmaak_f32 v153, v153, v187, 0x358637bd
	v_rsq_f32_e32 v146, v146
	v_rsq_f32_e32 v147, v147
	v_rsq_f32_e32 v148, v148
	v_rsq_f32_e32 v149, v149
	v_rsq_f32_e32 v150, v150
	v_rsq_f32_e32 v151, v151
	v_rsq_f32_e32 v152, v152
	v_rsq_f32_e32 v153, v153
	s_nop 0
	v_mul_f32_e32 v106, v106, v146
	v_mul_f32_e32 v107, v107, v146
	v_mul_f32_e32 v108, v108, v146
	v_mul_f32_e32 v109, v109, v146
	v_mul_f32_e32 v106, v178, v106
	v_mul_f32_e32 v107, v179, v107
	v_mul_f32_e32 v108, v180, v108
	v_mul_f32_e32 v109, v181, v109
	v_cvt_pk_bf16_f32 v106, v106, v106
	v_cvt_pk_bf16_f32 v107, v107, v107
	v_cvt_pk_bf16_f32 v108, v108, v108
	v_cvt_pk_bf16_f32 v109, v109, v109
	ds_write_b16 v183, v106 offset:4352
	ds_write_b16 v183, v107 offset:4416
	ds_write_b16 v183, v108 offset:4480
	ds_write_b16 v183, v109 offset:4544
	v_mul_f32_e32 v110, v110, v147
	v_mul_f32_e32 v111, v111, v147
	v_mul_f32_e32 v112, v112, v147
	v_mul_f32_e32 v113, v113, v147
	v_mul_f32_e32 v110, v178, v110
	v_mul_f32_e32 v111, v179, v111
	v_mul_f32_e32 v112, v180, v112
	v_mul_f32_e32 v113, v181, v113
	v_cvt_pk_bf16_f32 v110, v110, v110
	v_cvt_pk_bf16_f32 v111, v111, v111
	v_cvt_pk_bf16_f32 v112, v112, v112
	v_cvt_pk_bf16_f32 v113, v113, v113
	ds_write_b16 v183, v110 offset:4624
	ds_write_b16 v183, v111 offset:4688
	ds_write_b16 v183, v112 offset:4752
	ds_write_b16 v183, v113 offset:4816
	v_mul_f32_e32 v114, v114, v148
	v_mul_f32_e32 v115, v115, v148
	v_mul_f32_e32 v116, v116, v148
	v_mul_f32_e32 v117, v117, v148
	v_mul_f32_e32 v114, v178, v114
	v_mul_f32_e32 v115, v179, v115
	v_mul_f32_e32 v116, v180, v116
	v_mul_f32_e32 v117, v181, v117
	v_cvt_pk_bf16_f32 v114, v114, v114
	v_cvt_pk_bf16_f32 v115, v115, v115
	v_cvt_pk_bf16_f32 v116, v116, v116
	v_cvt_pk_bf16_f32 v117, v117, v117
	ds_write_b16 v183, v114 offset:4896
	ds_write_b16 v183, v115 offset:4960
	ds_write_b16 v183, v116 offset:5024
	ds_write_b16 v183, v117 offset:5088
	v_mul_f32_e32 v118, v118, v149
	v_mul_f32_e32 v119, v119, v149
	v_mul_f32_e32 v120, v120, v149
	v_mul_f32_e32 v121, v121, v149
	v_mul_f32_e32 v118, v178, v118
	v_mul_f32_e32 v119, v179, v119
	v_mul_f32_e32 v120, v180, v120
	v_mul_f32_e32 v121, v181, v121
	v_cvt_pk_bf16_f32 v118, v118, v118
	v_cvt_pk_bf16_f32 v119, v119, v119
	v_cvt_pk_bf16_f32 v120, v120, v120
	v_cvt_pk_bf16_f32 v121, v121, v121
	ds_write_b16 v183, v118 offset:5168
	ds_write_b16 v183, v119 offset:5232
	ds_write_b16 v183, v120 offset:5296
	s_waitcnt lgkmcnt(14)
	ds_write_b16 v183, v121 offset:5360
	v_mul_f32_e32 v122, v122, v150
	v_mul_f32_e32 v123, v123, v150
	v_mul_f32_e32 v124, v124, v150
	v_mul_f32_e32 v125, v125, v150
	v_mul_f32_e32 v122, v178, v122
	v_mul_f32_e32 v123, v179, v123
	v_mul_f32_e32 v124, v180, v124
	v_mul_f32_e32 v125, v181, v125
	v_cvt_pk_bf16_f32 v122, v122, v122
	v_cvt_pk_bf16_f32 v123, v123, v123
	v_cvt_pk_bf16_f32 v124, v124, v124
	v_cvt_pk_bf16_f32 v125, v125, v125
	s_waitcnt lgkmcnt(14)
	ds_write_b16 v183, v122 offset:6528
	s_waitcnt lgkmcnt(14)
	ds_write_b16 v183, v123 offset:6592
	s_waitcnt lgkmcnt(14)
	ds_write_b16 v183, v124 offset:6656
	s_waitcnt lgkmcnt(14)
	ds_write_b16 v183, v125 offset:6720
	v_mul_f32_e32 v126, v126, v151
	v_mul_f32_e32 v127, v127, v151
	v_mul_f32_e32 v128, v128, v151
	v_mul_f32_e32 v129, v129, v151
	v_mul_f32_e32 v126, v178, v126
	v_mul_f32_e32 v127, v179, v127
	v_mul_f32_e32 v128, v180, v128
	v_mul_f32_e32 v129, v181, v129
	v_cvt_pk_bf16_f32 v126, v126, v126
	v_cvt_pk_bf16_f32 v127, v127, v127
	v_cvt_pk_bf16_f32 v128, v128, v128
	v_cvt_pk_bf16_f32 v129, v129, v129
	s_waitcnt lgkmcnt(14)
	ds_write_b16 v183, v126 offset:6800
	s_waitcnt lgkmcnt(14)
	ds_write_b16 v183, v127 offset:6864
	s_waitcnt lgkmcnt(14)
	ds_write_b16 v183, v128 offset:6928
	s_waitcnt lgkmcnt(14)
	ds_write_b16 v183, v129 offset:6992
	v_mul_f32_e32 v130, v130, v152
	v_mul_f32_e32 v131, v131, v152
	v_mul_f32_e32 v132, v132, v152
	v_mul_f32_e32 v133, v133, v152
	v_mul_f32_e32 v130, v178, v130
	v_mul_f32_e32 v131, v179, v131
	v_mul_f32_e32 v132, v180, v132
	v_mul_f32_e32 v133, v181, v133
	v_cvt_pk_bf16_f32 v130, v130, v130
	v_cvt_pk_bf16_f32 v131, v131, v131
	v_cvt_pk_bf16_f32 v132, v132, v132
	v_cvt_pk_bf16_f32 v133, v133, v133
	s_waitcnt lgkmcnt(14)
	ds_write_b16 v183, v130 offset:7072
	s_waitcnt lgkmcnt(14)
	ds_write_b16 v183, v131 offset:7136
	s_waitcnt lgkmcnt(14)
	ds_write_b16 v183, v132 offset:7200
	s_waitcnt lgkmcnt(14)
	ds_write_b16 v183, v133 offset:7264
	v_mul_f32_e32 v134, v134, v153
	v_mul_f32_e32 v135, v135, v153
	v_mul_f32_e32 v136, v136, v153
	v_mul_f32_e32 v137, v137, v153
	v_mul_f32_e32 v134, v178, v134
	v_mul_f32_e32 v135, v179, v135
	v_mul_f32_e32 v136, v180, v136
	v_mul_f32_e32 v137, v181, v137
	v_cvt_pk_bf16_f32 v134, v134, v134
	v_cvt_pk_bf16_f32 v135, v135, v135
	v_cvt_pk_bf16_f32 v136, v136, v136
	v_cvt_pk_bf16_f32 v137, v137, v137
	s_waitcnt lgkmcnt(14)
	ds_write_b16 v183, v134 offset:7344
	s_waitcnt lgkmcnt(14)
	ds_write_b16 v183, v135 offset:7408
	s_waitcnt lgkmcnt(14)
	ds_write_b16 v183, v136 offset:7472
	s_waitcnt lgkmcnt(14)
	ds_write_b16 v183, v137 offset:7536
	s_waitcnt lgkmcnt(0)
	ds_read_b128 v[106:109], v185 offset:0
	ds_read_b128 v[110:113], v185 offset:1088
	ds_read_b128 v[114:117], v185 offset:2176
	ds_read_b128 v[118:121], v185 offset:3264
	ds_read_b128 v[122:125], v185 offset:4352
	ds_read_b128 v[126:129], v185 offset:5440
	ds_read_b128 v[130:133], v185 offset:6528
	ds_read_b128 v[134:137], v185 offset:7616
	s_waitcnt lgkmcnt(7)
	global_store_dwordx4 v186, v[106:109], s[42:43]
	s_add_u32 s42, s42, 0x2000
	s_addc_u32 s43, s43, 0
	s_waitcnt lgkmcnt(6)
	global_store_dwordx4 v186, v[110:113], s[42:43]
	s_add_u32 s42, s42, 0x2000
	s_addc_u32 s43, s43, 0
	s_waitcnt lgkmcnt(5)
	global_store_dwordx4 v186, v[114:117], s[42:43]
	s_add_u32 s42, s42, 0x2000
	s_addc_u32 s43, s43, 0
	s_waitcnt lgkmcnt(4)
	global_store_dwordx4 v186, v[118:121], s[42:43]
	s_add_u32 s42, s42, 0x2000
	s_addc_u32 s43, s43, 0
	s_waitcnt lgkmcnt(3)
	global_store_dwordx4 v186, v[122:125], s[42:43]
	s_add_u32 s42, s42, 0x2000
	s_addc_u32 s43, s43, 0
	s_waitcnt lgkmcnt(2)
	global_store_dwordx4 v186, v[126:129], s[42:43]
	s_add_u32 s42, s42, 0x2000
	s_addc_u32 s43, s43, 0
	s_waitcnt lgkmcnt(1)
	global_store_dwordx4 v186, v[130:133], s[42:43]
	s_add_u32 s42, s42, 0x2000
	s_addc_u32 s43, s43, 0
	s_waitcnt lgkmcnt(0)
	global_store_dwordx4 v186, v[134:137], s[42:43]
